# mix_post (both layers): per-wave item loop unrolled x4 with all loads issued first, ln_w/ln_b hoisted
# speedup vs baseline: 1.0084x; 1.0084x over previous
.LBB0_783:
	s_or_b64 exec, exec, s[4:5]
	v_mov_b32_e32 v1, s2
	s_waitcnt lgkmcnt(0)
	s_barrier
	v_mbcnt_lo_u32_b32 v0, -1, 0
	v_mbcnt_hi_u32_b32 v0, -1, v0
	s_nop 0
	v_readfirstlane_b32 s16, v1
	v_mov_b32_e32 v1, 0
	s_load_dwordx2 s[4:5], s[52:53], 0x188
	s_lshl_b32 s0, s16, 3
	s_add_i32 s18, s0, s66
	s_cmpk_gt_i32 s18, 0x7fff
	v_readfirstlane_b32 s6, v1
	s_cbranch_scc1 .LBB0_787
	s_ashr_i32 s0, s6, 31
	s_waitcnt lgkmcnt(0)
	s_add_u32 s1, s4, s6
	s_addc_u32 s0, s5, s0
	s_add_u32 s6, s1, 0x4c480000
	s_addc_u32 s7, s0, 0
	s_add_u32 s12, s1, 0x48480000
	s_addc_u32 s13, s0, 0
	s_add_u32 s14, s1, 0x4a480000
	s_addc_u32 s15, s0, 0
	s_load_dwordx4 s[8:11], s[52:53], 0x78
	s_add_u32 s19, s1, 0x4c0000
	s_addc_u32 s20, s0, 0
	s_add_u32 s21, s1, 0x35c80000
	s_addc_u32 s22, s0, 0
	s_lshl_b32 s0, s16, 11
	s_lshl_b32 s1, s66, 8
	v_lshlrev_b32_e32 v0, 2, v0
	s_add_i32 s23, s0, s1
	v_mov_b32_e32 v1, 0x3a27c5ac
	s_mov_b32 s24, 0xf800000
	v_mov_b32_e32 v2, 0x260
	s_waitcnt lgkmcnt(0)
	s_and_b32 s0, s23, 0x300
	v_add_u32_e32 v130, s0, v0
	v_lshlrev_b32_e32 v130, 2, v130
	global_load_dwordx4 v[134:137], v130, s[10:11]
	global_load_dwordx4 v[130:133], v130, s[8:9]
.LBB0_785:
	s_ashr_i32 s4, s18, 2
	s_and_b32 s0, s23, 0x300
	v_add_u32_e32 v16, s0, v0
	s_ashr_i32 s5, s4, 31
	s_lshl_b64 s[16:17], s[4:5], 10
	v_ashrrev_i32_e32 v17, 31, v16
	v_lshl_add_u64 v[4:5], s[16:17], 0, v[16:17]
	v_lshl_add_u64 v[8:9], v[4:5], 2, s[6:7]
	v_lshlrev_b64 v[10:11], 1, v[4:5]
	s_waitcnt lgkmcnt(0)
	global_load_dwordx4 v[4:7], v[8:9], off
	s_lshl_b64 s[26:27], s[4:5], 6
	v_ashrrev_i32_e32 v18, 6, v16
	s_add_u32 s16, s19, s26
	v_ashrrev_i32_e32 v19, 31, v18
	s_addc_u32 s17, s20, s27
	v_lshl_add_u64 v[20:21], s[12:13], 0, v[10:11]
	v_lshl_add_u64 v[22:23], s[14:15], 0, v[10:11]
	s_nop 0
	v_lshl_add_u64 v[18:19], v[18:19], 2, s[16:17]
	global_load_dwordx2 v[20:21], v[20:21], off
	s_nop 0
	global_load_dwordx2 v[22:23], v[22:23], off
	s_nop 0
	global_load_dword v18, v[18:19], off
	s_lshl_b64 s[4:5], s[4:5], 12
	s_add_u32 s4, s21, s4
	s_addc_u32 s5, s22, s5
	v_lshl_add_u64 v[16:17], v[16:17], 1, s[4:5]
	s_add_i32 s0, s18, 0x800
	s_add_i32 s23, s23, 0x80000
	s_cmpk_lt_i32 s18, 0x7800
	s_mov_b32 s18, s0
	s_ashr_i32 s4, s18, 2
	s_and_b32 s0, s23, 0x300
	v_add_u32_e32 v48, s0, v0
	s_ashr_i32 s5, s4, 31
	s_lshl_b64 s[16:17], s[4:5], 10
	v_ashrrev_i32_e32 v49, 31, v48
	v_lshl_add_u64 v[36:37], s[16:17], 0, v[48:49]
	v_lshl_add_u64 v[40:41], v[36:37], 2, s[6:7]
	v_lshlrev_b64 v[42:43], 1, v[36:37]
	s_waitcnt lgkmcnt(0)
	global_load_dwordx4 v[36:39], v[40:41], off
	s_lshl_b64 s[26:27], s[4:5], 6
	v_ashrrev_i32_e32 v50, 6, v48
	s_add_u32 s16, s19, s26
	v_ashrrev_i32_e32 v51, 31, v50
	s_addc_u32 s17, s20, s27
	v_lshl_add_u64 v[52:53], s[12:13], 0, v[42:43]
	v_lshl_add_u64 v[54:55], s[14:15], 0, v[42:43]
	s_nop 0
	v_lshl_add_u64 v[50:51], v[50:51], 2, s[16:17]
	global_load_dwordx2 v[52:53], v[52:53], off
	s_nop 0
	global_load_dwordx2 v[54:55], v[54:55], off
	s_nop 0
	global_load_dword v50, v[50:51], off
	s_lshl_b64 s[4:5], s[4:5], 12
	s_add_u32 s4, s21, s4
	s_addc_u32 s5, s22, s5
	v_lshl_add_u64 v[48:49], v[48:49], 1, s[4:5]
	s_add_i32 s0, s18, 0x800
	s_add_i32 s23, s23, 0x80000
	s_cmpk_lt_i32 s18, 0x7800
	s_mov_b32 s18, s0
	s_ashr_i32 s4, s18, 2
	s_and_b32 s0, s23, 0x300
	v_add_u32_e32 v80, s0, v0
	s_ashr_i32 s5, s4, 31
	s_lshl_b64 s[16:17], s[4:5], 10
	v_ashrrev_i32_e32 v81, 31, v80
	v_lshl_add_u64 v[68:69], s[16:17], 0, v[80:81]
	v_lshl_add_u64 v[72:73], v[68:69], 2, s[6:7]
	v_lshlrev_b64 v[74:75], 1, v[68:69]
	s_waitcnt lgkmcnt(0)
	global_load_dwordx4 v[68:71], v[72:73], off
	s_lshl_b64 s[26:27], s[4:5], 6
	v_ashrrev_i32_e32 v82, 6, v80
	s_add_u32 s16, s19, s26
	v_ashrrev_i32_e32 v83, 31, v82
	s_addc_u32 s17, s20, s27
	v_lshl_add_u64 v[84:85], s[12:13], 0, v[74:75]
	v_lshl_add_u64 v[86:87], s[14:15], 0, v[74:75]
	s_nop 0
	v_lshl_add_u64 v[82:83], v[82:83], 2, s[16:17]
	global_load_dwordx2 v[84:85], v[84:85], off
	s_nop 0
	global_load_dwordx2 v[86:87], v[86:87], off
	s_nop 0
	global_load_dword v82, v[82:83], off
	s_lshl_b64 s[4:5], s[4:5], 12
	s_add_u32 s4, s21, s4
	s_addc_u32 s5, s22, s5
	v_lshl_add_u64 v[80:81], v[80:81], 1, s[4:5]
	s_add_i32 s0, s18, 0x800
	s_add_i32 s23, s23, 0x80000
	s_cmpk_lt_i32 s18, 0x7800
	s_mov_b32 s18, s0
	s_ashr_i32 s4, s18, 2
	s_and_b32 s0, s23, 0x300
	v_add_u32_e32 v112, s0, v0
	s_ashr_i32 s5, s4, 31
	s_lshl_b64 s[16:17], s[4:5], 10
	v_ashrrev_i32_e32 v113, 31, v112
	v_lshl_add_u64 v[100:101], s[16:17], 0, v[112:113]
	v_lshl_add_u64 v[104:105], v[100:101], 2, s[6:7]
	v_lshlrev_b64 v[106:107], 1, v[100:101]
	s_waitcnt lgkmcnt(0)
	global_load_dwordx4 v[100:103], v[104:105], off
	s_lshl_b64 s[26:27], s[4:5], 6
	v_ashrrev_i32_e32 v114, 6, v112
	s_add_u32 s16, s19, s26
	v_ashrrev_i32_e32 v115, 31, v114
	s_addc_u32 s17, s20, s27
	v_lshl_add_u64 v[116:117], s[12:13], 0, v[106:107]
	v_lshl_add_u64 v[118:119], s[14:15], 0, v[106:107]
	s_nop 0
	v_lshl_add_u64 v[114:115], v[114:115], 2, s[16:17]
	global_load_dwordx2 v[116:117], v[116:117], off
	s_nop 0
	global_load_dwordx2 v[118:119], v[118:119], off
	s_nop 0
	global_load_dword v114, v[114:115], off
	s_lshl_b64 s[4:5], s[4:5], 12
	s_add_u32 s4, s21, s4
	s_addc_u32 s5, s22, s5
	v_lshl_add_u64 v[112:113], v[112:113], 1, s[4:5]
	s_add_i32 s0, s18, 0x800
	s_add_i32 s23, s23, 0x80000
	s_cmpk_lt_i32 s18, 0x7800
	s_mov_b32 s18, s0
	s_waitcnt vmcnt(15)
	v_mov_b32_e32 v24, v5
	v_mov_b32_e32 v25, v6
	v_mov_b32_e32 v26, v4
	v_mov_b32_e32 v27, v7
	v_pk_add_f32 v[24:25], v[24:25], v[26:27]
	s_waitcnt vmcnt(14)
	v_lshlrev_b32_e32 v26, 16, v20
	v_add_f32_e32 v3, v24, v25
	v_and_b32_e32 v27, 0xffff0000, v20
	v_lshlrev_b32_e32 v20, 16, v21
	v_add_f32_dpp v3, v3, v3 quad_perm:[1,0,3,2] row_mask:0xf bank_mask:0xf bound_ctrl:1
	v_and_b32_e32 v21, 0xffff0000, v21
	s_waitcnt vmcnt(13)
	v_lshlrev_b32_e32 v28, 16, v22
	v_add_f32_dpp v3, v3, v3 quad_perm:[2,3,0,1] row_mask:0xf bank_mask:0xf bound_ctrl:1
	v_and_b32_e32 v29, 0xffff0000, v22
	v_lshlrev_b32_e32 v22, 16, v23
	v_add_f32_dpp v3, v3, v3 row_half_mirror row_mask:0xf bank_mask:0xf bound_ctrl:1
	v_and_b32_e32 v23, 0xffff0000, v23
	s_nop 0
	v_add_f32_dpp v3, v3, v3 row_mirror row_mask:0xf bank_mask:0xf bound_ctrl:1
	v_fmamk_f32 v5, v3, 0xbc800000, v5
	v_fmamk_f32 v4, v3, 0xbc800000, v4
	v_fmamk_f32 v7, v3, 0xbc800000, v7
	v_fmac_f32_e32 v6, 0xbc800000, v3
	v_pk_mul_f32 v[24:25], v[6:7], v[6:7]
	v_pk_mul_f32 v[30:31], v[4:5], v[4:5]
	s_nop 0
	v_pk_mov_b32 v[32:33], v[30:31], v[24:25] op_sel:[1,0]
	v_mov_b32_e32 v31, v25
	v_pk_add_f32 v[24:25], v[32:33], v[30:31]
	s_nop 0
	v_add_f32_e32 v3, v24, v25
	s_nop 1
	v_add_f32_dpp v3, v3, v3 quad_perm:[1,0,3,2] row_mask:0xf bank_mask:0xf bound_ctrl:1
	s_nop 1
	v_add_f32_dpp v3, v3, v3 quad_perm:[2,3,0,1] row_mask:0xf bank_mask:0xf bound_ctrl:1
	s_nop 1
	v_add_f32_dpp v3, v3, v3 row_half_mirror row_mask:0xf bank_mask:0xf bound_ctrl:1
	s_nop 1
	v_add_f32_dpp v3, v3, v3 row_mirror row_mask:0xf bank_mask:0xf bound_ctrl:1
	v_fmamk_f32 v3, v3, 0x3c800000, v1
	v_mul_f32_e32 v19, 0x4f800000, v3
	v_cmp_gt_f32_e32 vcc, s24, v3
	s_nop 1
	v_cndmask_b32_e32 v3, v3, v19, vcc
	v_sqrt_f32_e32 v19, v3
	s_nop 0
	v_add_u32_e32 v24, -1, v19
	v_add_u32_e32 v25, 1, v19
	v_fma_f32 v30, -v24, v19, v3
	v_fma_f32 v31, -v25, v19, v3
	v_cmp_ge_f32_e64 s[4:5], 0, v30
	s_nop 1
	v_cndmask_b32_e64 v19, v19, v24, s[4:5]
	v_cmp_lt_f32_e64 s[4:5], 0, v31
	s_nop 1
	v_cndmask_b32_e64 v19, v19, v25, s[4:5]
	v_mul_f32_e32 v24, 0x37800000, v19
	v_cndmask_b32_e32 v19, v19, v24, vcc
	v_cmp_class_f32_e32 vcc, v3, v2
	s_nop 1
	v_cndmask_b32_e32 v3, v19, v3, vcc
	v_div_scale_f32 v19, s[4:5], v3, v3, 1.0
	v_rcp_f32_e32 v25, v19
	v_div_scale_f32 v24, vcc, 1.0, v3, 1.0
	v_fma_f32 v30, -v19, v25, 1.0
	v_fmac_f32_e32 v25, v30, v25
	v_mul_f32_e32 v30, v24, v25
	v_fma_f32 v31, -v19, v30, v24
	v_fmac_f32_e32 v30, v31, v25
	v_fma_f32 v19, -v19, v30, v24
	v_div_fmas_f32 v19, v19, v25, v30
	v_div_fixup_f32 v24, v19, v3, 1.0
	v_pk_mul_f32 v[4:5], v[4:5], v[24:25] op_sel_hi:[1,0]
	v_pk_mul_f32 v[6:7], v[6:7], v[24:25] op_sel_hi:[1,0]
	v_pk_fma_f32 v[4:5], v[130:131], v[4:5], v[134:135]
	v_pk_fma_f32 v[6:7], v[132:133], v[6:7], v[136:137]
	s_waitcnt vmcnt(12)
	v_pk_fma_f32 v[4:5], v[18:19], v[26:27], v[4:5] op_sel_hi:[0,1,1]
	v_pk_fma_f32 v[6:7], v[18:19], v[20:21], v[6:7] op_sel_hi:[0,1,1]
	v_pk_mul_f32 v[6:7], v[6:7], v[22:23]
	v_pk_mul_f32 v[4:5], v[4:5], v[28:29]
	s_nop 0
	v_cvt_pk_bf16_f32 v4, v4, v5
	v_cvt_pk_bf16_f32 v5, v6, v7
	global_store_dwordx2 v[16:17], v[4:5], off
	s_waitcnt vmcnt(12)
	v_mov_b32_e32 v56, v37
	v_mov_b32_e32 v57, v38
	v_mov_b32_e32 v58, v36
	v_mov_b32_e32 v59, v39
	v_pk_add_f32 v[56:57], v[56:57], v[58:59]
	s_waitcnt vmcnt(11)
	v_lshlrev_b32_e32 v58, 16, v52
	v_add_f32_e32 v35, v56, v57
	v_and_b32_e32 v59, 0xffff0000, v52
	v_lshlrev_b32_e32 v52, 16, v53
	v_add_f32_dpp v35, v35, v35 quad_perm:[1,0,3,2] row_mask:0xf bank_mask:0xf bound_ctrl:1
	v_and_b32_e32 v53, 0xffff0000, v53
	s_waitcnt vmcnt(10)
	v_lshlrev_b32_e32 v60, 16, v54
	v_add_f32_dpp v35, v35, v35 quad_perm:[2,3,0,1] row_mask:0xf bank_mask:0xf bound_ctrl:1
	v_and_b32_e32 v61, 0xffff0000, v54
	v_lshlrev_b32_e32 v54, 16, v55
	v_add_f32_dpp v35, v35, v35 row_half_mirror row_mask:0xf bank_mask:0xf bound_ctrl:1
	v_and_b32_e32 v55, 0xffff0000, v55
	s_nop 0
	v_add_f32_dpp v35, v35, v35 row_mirror row_mask:0xf bank_mask:0xf bound_ctrl:1
	v_fmamk_f32 v37, v35, 0xbc800000, v37
	v_fmamk_f32 v36, v35, 0xbc800000, v36
	v_fmamk_f32 v39, v35, 0xbc800000, v39
	v_fmac_f32_e32 v38, 0xbc800000, v35
	v_pk_mul_f32 v[56:57], v[38:39], v[38:39]
	v_pk_mul_f32 v[62:63], v[36:37], v[36:37]
	s_nop 0
	v_pk_mov_b32 v[64:65], v[62:63], v[56:57] op_sel:[1,0]
	v_mov_b32_e32 v63, v57
	v_pk_add_f32 v[56:57], v[64:65], v[62:63]
	s_nop 0
	v_add_f32_e32 v35, v56, v57
	s_nop 1
	v_add_f32_dpp v35, v35, v35 quad_perm:[1,0,3,2] row_mask:0xf bank_mask:0xf bound_ctrl:1
	s_nop 1
	v_add_f32_dpp v35, v35, v35 quad_perm:[2,3,0,1] row_mask:0xf bank_mask:0xf bound_ctrl:1
	s_nop 1
	v_add_f32_dpp v35, v35, v35 row_half_mirror row_mask:0xf bank_mask:0xf bound_ctrl:1
	s_nop 1
	v_add_f32_dpp v35, v35, v35 row_mirror row_mask:0xf bank_mask:0xf bound_ctrl:1
	v_fmamk_f32 v35, v35, 0x3c800000, v1
	v_mul_f32_e32 v51, 0x4f800000, v35
	v_cmp_gt_f32_e32 vcc, s24, v35
	s_nop 1
	v_cndmask_b32_e32 v35, v35, v51, vcc
	v_sqrt_f32_e32 v51, v35
	s_nop 0
	v_add_u32_e32 v56, -1, v51
	v_add_u32_e32 v57, 1, v51
	v_fma_f32 v62, -v56, v51, v35
	v_fma_f32 v63, -v57, v51, v35
	v_cmp_ge_f32_e64 s[4:5], 0, v62
	s_nop 1
	v_cndmask_b32_e64 v51, v51, v56, s[4:5]
	v_cmp_lt_f32_e64 s[4:5], 0, v63
	s_nop 1
	v_cndmask_b32_e64 v51, v51, v57, s[4:5]
	v_mul_f32_e32 v56, 0x37800000, v51
	v_cndmask_b32_e32 v51, v51, v56, vcc
	v_cmp_class_f32_e32 vcc, v35, v2
	s_nop 1
	v_cndmask_b32_e32 v35, v51, v35, vcc
	v_div_scale_f32 v51, s[4:5], v35, v35, 1.0
	v_rcp_f32_e32 v57, v51
	v_div_scale_f32 v56, vcc, 1.0, v35, 1.0
	v_fma_f32 v62, -v51, v57, 1.0
	v_fmac_f32_e32 v57, v62, v57
	v_mul_f32_e32 v62, v56, v57
	v_fma_f32 v63, -v51, v62, v56
	v_fmac_f32_e32 v62, v63, v57
	v_fma_f32 v51, -v51, v62, v56
	v_div_fmas_f32 v51, v51, v57, v62
	v_div_fixup_f32 v56, v51, v35, 1.0
	v_pk_mul_f32 v[36:37], v[36:37], v[56:57] op_sel_hi:[1,0]
	v_pk_mul_f32 v[38:39], v[38:39], v[56:57] op_sel_hi:[1,0]
	v_pk_fma_f32 v[36:37], v[130:131], v[36:37], v[134:135]
	v_pk_fma_f32 v[38:39], v[132:133], v[38:39], v[136:137]
	s_waitcnt vmcnt(9)
	v_pk_fma_f32 v[36:37], v[50:51], v[58:59], v[36:37] op_sel_hi:[0,1,1]
	v_pk_fma_f32 v[38:39], v[50:51], v[52:53], v[38:39] op_sel_hi:[0,1,1]
	v_pk_mul_f32 v[38:39], v[38:39], v[54:55]
	v_pk_mul_f32 v[36:37], v[36:37], v[60:61]
	s_nop 0
	v_cvt_pk_bf16_f32 v36, v36, v37
	v_cvt_pk_bf16_f32 v37, v38, v39
	global_store_dwordx2 v[48:49], v[36:37], off
	s_waitcnt vmcnt(9)
	v_mov_b32_e32 v88, v69
	v_mov_b32_e32 v89, v70
	v_mov_b32_e32 v90, v68
	v_mov_b32_e32 v91, v71
	v_pk_add_f32 v[88:89], v[88:89], v[90:91]
	s_waitcnt vmcnt(8)
	v_lshlrev_b32_e32 v90, 16, v84
	v_add_f32_e32 v67, v88, v89
	v_and_b32_e32 v91, 0xffff0000, v84
	v_lshlrev_b32_e32 v84, 16, v85
	v_add_f32_dpp v67, v67, v67 quad_perm:[1,0,3,2] row_mask:0xf bank_mask:0xf bound_ctrl:1
	v_and_b32_e32 v85, 0xffff0000, v85
	s_waitcnt vmcnt(7)
	v_lshlrev_b32_e32 v92, 16, v86
	v_add_f32_dpp v67, v67, v67 quad_perm:[2,3,0,1] row_mask:0xf bank_mask:0xf bound_ctrl:1
	v_and_b32_e32 v93, 0xffff0000, v86
	v_lshlrev_b32_e32 v86, 16, v87
	v_add_f32_dpp v67, v67, v67 row_half_mirror row_mask:0xf bank_mask:0xf bound_ctrl:1
	v_and_b32_e32 v87, 0xffff0000, v87
	s_nop 0
	v_add_f32_dpp v67, v67, v67 row_mirror row_mask:0xf bank_mask:0xf bound_ctrl:1
	v_fmamk_f32 v69, v67, 0xbc800000, v69
	v_fmamk_f32 v68, v67, 0xbc800000, v68
	v_fmamk_f32 v71, v67, 0xbc800000, v71
	v_fmac_f32_e32 v70, 0xbc800000, v67
	v_pk_mul_f32 v[88:89], v[70:71], v[70:71]
	v_pk_mul_f32 v[94:95], v[68:69], v[68:69]
	s_nop 0
	v_pk_mov_b32 v[96:97], v[94:95], v[88:89] op_sel:[1,0]
	v_mov_b32_e32 v95, v89
	v_pk_add_f32 v[88:89], v[96:97], v[94:95]
	s_nop 0
	v_add_f32_e32 v67, v88, v89
	s_nop 1
	v_add_f32_dpp v67, v67, v67 quad_perm:[1,0,3,2] row_mask:0xf bank_mask:0xf bound_ctrl:1
	s_nop 1
	v_add_f32_dpp v67, v67, v67 quad_perm:[2,3,0,1] row_mask:0xf bank_mask:0xf bound_ctrl:1
	s_nop 1
	v_add_f32_dpp v67, v67, v67 row_half_mirror row_mask:0xf bank_mask:0xf bound_ctrl:1
	s_nop 1
	v_add_f32_dpp v67, v67, v67 row_mirror row_mask:0xf bank_mask:0xf bound_ctrl:1
	v_fmamk_f32 v67, v67, 0x3c800000, v1
	v_mul_f32_e32 v83, 0x4f800000, v67
	v_cmp_gt_f32_e32 vcc, s24, v67
	s_nop 1
	v_cndmask_b32_e32 v67, v67, v83, vcc
	v_sqrt_f32_e32 v83, v67
	s_nop 0
	v_add_u32_e32 v88, -1, v83
	v_add_u32_e32 v89, 1, v83
	v_fma_f32 v94, -v88, v83, v67
	v_fma_f32 v95, -v89, v83, v67
	v_cmp_ge_f32_e64 s[4:5], 0, v94
	s_nop 1
	v_cndmask_b32_e64 v83, v83, v88, s[4:5]
	v_cmp_lt_f32_e64 s[4:5], 0, v95
	s_nop 1
	v_cndmask_b32_e64 v83, v83, v89, s[4:5]
	v_mul_f32_e32 v88, 0x37800000, v83
	v_cndmask_b32_e32 v83, v83, v88, vcc
	v_cmp_class_f32_e32 vcc, v67, v2
	s_nop 1
	v_cndmask_b32_e32 v67, v83, v67, vcc
	v_div_scale_f32 v83, s[4:5], v67, v67, 1.0
	v_rcp_f32_e32 v89, v83
	v_div_scale_f32 v88, vcc, 1.0, v67, 1.0
	v_fma_f32 v94, -v83, v89, 1.0
	v_fmac_f32_e32 v89, v94, v89
	v_mul_f32_e32 v94, v88, v89
	v_fma_f32 v95, -v83, v94, v88
	v_fmac_f32_e32 v94, v95, v89
	v_fma_f32 v83, -v83, v94, v88
	v_div_fmas_f32 v83, v83, v89, v94
	v_div_fixup_f32 v88, v83, v67, 1.0
	v_pk_mul_f32 v[68:69], v[68:69], v[88:89] op_sel_hi:[1,0]
	v_pk_mul_f32 v[70:71], v[70:71], v[88:89] op_sel_hi:[1,0]
	v_pk_fma_f32 v[68:69], v[130:131], v[68:69], v[134:135]
	v_pk_fma_f32 v[70:71], v[132:133], v[70:71], v[136:137]
	s_waitcnt vmcnt(6)
	v_pk_fma_f32 v[68:69], v[82:83], v[90:91], v[68:69] op_sel_hi:[0,1,1]
	v_pk_fma_f32 v[70:71], v[82:83], v[84:85], v[70:71] op_sel_hi:[0,1,1]
	v_pk_mul_f32 v[70:71], v[70:71], v[86:87]
	v_pk_mul_f32 v[68:69], v[68:69], v[92:93]
	s_nop 0
	v_cvt_pk_bf16_f32 v68, v68, v69
	v_cvt_pk_bf16_f32 v69, v70, v71
	global_store_dwordx2 v[80:81], v[68:69], off
	s_waitcnt vmcnt(6)
	v_mov_b32_e32 v120, v101
	v_mov_b32_e32 v121, v102
	v_mov_b32_e32 v122, v100
	v_mov_b32_e32 v123, v103
	v_pk_add_f32 v[120:121], v[120:121], v[122:123]
	s_waitcnt vmcnt(5)
	v_lshlrev_b32_e32 v122, 16, v116
	v_add_f32_e32 v99, v120, v121
	v_and_b32_e32 v123, 0xffff0000, v116
	v_lshlrev_b32_e32 v116, 16, v117
	v_add_f32_dpp v99, v99, v99 quad_perm:[1,0,3,2] row_mask:0xf bank_mask:0xf bound_ctrl:1
	v_and_b32_e32 v117, 0xffff0000, v117
	s_waitcnt vmcnt(4)
	v_lshlrev_b32_e32 v124, 16, v118
	v_add_f32_dpp v99, v99, v99 quad_perm:[2,3,0,1] row_mask:0xf bank_mask:0xf bound_ctrl:1
	v_and_b32_e32 v125, 0xffff0000, v118
	v_lshlrev_b32_e32 v118, 16, v119
	v_add_f32_dpp v99, v99, v99 row_half_mirror row_mask:0xf bank_mask:0xf bound_ctrl:1
	v_and_b32_e32 v119, 0xffff0000, v119
	s_nop 0
	v_add_f32_dpp v99, v99, v99 row_mirror row_mask:0xf bank_mask:0xf bound_ctrl:1
	v_fmamk_f32 v101, v99, 0xbc800000, v101
	v_fmamk_f32 v100, v99, 0xbc800000, v100
	v_fmamk_f32 v103, v99, 0xbc800000, v103
	v_fmac_f32_e32 v102, 0xbc800000, v99
	v_pk_mul_f32 v[120:121], v[102:103], v[102:103]
	v_pk_mul_f32 v[126:127], v[100:101], v[100:101]
	s_nop 0
	v_pk_mov_b32 v[128:129], v[126:127], v[120:121] op_sel:[1,0]
	v_mov_b32_e32 v127, v121
	v_pk_add_f32 v[120:121], v[128:129], v[126:127]
	s_nop 0
	v_add_f32_e32 v99, v120, v121
	s_nop 1
	v_add_f32_dpp v99, v99, v99 quad_perm:[1,0,3,2] row_mask:0xf bank_mask:0xf bound_ctrl:1
	s_nop 1
	v_add_f32_dpp v99, v99, v99 quad_perm:[2,3,0,1] row_mask:0xf bank_mask:0xf bound_ctrl:1
	s_nop 1
	v_add_f32_dpp v99, v99, v99 row_half_mirror row_mask:0xf bank_mask:0xf bound_ctrl:1
	s_nop 1
	v_add_f32_dpp v99, v99, v99 row_mirror row_mask:0xf bank_mask:0xf bound_ctrl:1
	v_fmamk_f32 v99, v99, 0x3c800000, v1
	v_mul_f32_e32 v115, 0x4f800000, v99
	v_cmp_gt_f32_e32 vcc, s24, v99
	s_nop 1
	v_cndmask_b32_e32 v99, v99, v115, vcc
	v_sqrt_f32_e32 v115, v99
	s_nop 0
	v_add_u32_e32 v120, -1, v115
	v_add_u32_e32 v121, 1, v115
	v_fma_f32 v126, -v120, v115, v99
	v_fma_f32 v127, -v121, v115, v99
	v_cmp_ge_f32_e64 s[4:5], 0, v126
	s_nop 1
	v_cndmask_b32_e64 v115, v115, v120, s[4:5]
	v_cmp_lt_f32_e64 s[4:5], 0, v127
	s_nop 1
	v_cndmask_b32_e64 v115, v115, v121, s[4:5]
	v_mul_f32_e32 v120, 0x37800000, v115
	v_cndmask_b32_e32 v115, v115, v120, vcc
	v_cmp_class_f32_e32 vcc, v99, v2
	s_nop 1
	v_cndmask_b32_e32 v99, v115, v99, vcc
	v_div_scale_f32 v115, s[4:5], v99, v99, 1.0
	v_rcp_f32_e32 v121, v115
	v_div_scale_f32 v120, vcc, 1.0, v99, 1.0
	v_fma_f32 v126, -v115, v121, 1.0
	v_fmac_f32_e32 v121, v126, v121
	v_mul_f32_e32 v126, v120, v121
	v_fma_f32 v127, -v115, v126, v120
	v_fmac_f32_e32 v126, v127, v121
	v_fma_f32 v115, -v115, v126, v120
	v_div_fmas_f32 v115, v115, v121, v126
	v_div_fixup_f32 v120, v115, v99, 1.0
	v_pk_mul_f32 v[100:101], v[100:101], v[120:121] op_sel_hi:[1,0]
	v_pk_mul_f32 v[102:103], v[102:103], v[120:121] op_sel_hi:[1,0]
	v_pk_fma_f32 v[100:101], v[130:131], v[100:101], v[134:135]
	v_pk_fma_f32 v[102:103], v[132:133], v[102:103], v[136:137]
	s_waitcnt vmcnt(3)
	v_pk_fma_f32 v[100:101], v[114:115], v[122:123], v[100:101] op_sel_hi:[0,1,1]
	v_pk_fma_f32 v[102:103], v[114:115], v[116:117], v[102:103] op_sel_hi:[0,1,1]
	v_pk_mul_f32 v[102:103], v[102:103], v[118:119]
	v_pk_mul_f32 v[100:101], v[100:101], v[124:125]
	s_nop 0
	v_cvt_pk_bf16_f32 v100, v100, v101
	v_cvt_pk_bf16_f32 v101, v102, v103
	global_store_dwordx2 v[112:113], v[100:101], off
	s_cbranch_scc1 .LBB0_785
	s_load_dwordx2 s[4:5], s[52:53], 0x188

.LBB0_1877:
	s_or_b64 exec, exec, s[4:5]
	v_mov_b32_e32 v1, s2
	s_waitcnt lgkmcnt(0)
	s_barrier
	v_mbcnt_lo_u32_b32 v0, -1, 0
	v_mbcnt_hi_u32_b32 v0, -1, v0
	v_readlane_b32 s0, v254, 18
	v_readfirstlane_b32 s16, v1
	v_mov_b32_e32 v1, 0
	v_readlane_b32 s1, v254, 19
	s_load_dwordx2 s[6:7], s[0:1], 0x188
	s_lshl_b32 s0, s16, 3
	s_add_i32 s18, s0, s76
	s_cmpk_gt_i32 s18, 0x7fff
	v_readfirstlane_b32 s4, v1
	s_cbranch_scc1 .LBB0_1881
	s_ashr_i32 s0, s4, 31
	s_waitcnt lgkmcnt(0)
	s_add_u32 s1, s6, s4
	v_readlane_b32 s4, v254, 18
	s_addc_u32 s0, s7, s0
	v_readlane_b32 s5, v254, 19
	s_load_dwordx4 s[8:11], s[4:5], 0x130
	s_add_u32 s4, s1, 0x4c480000
	s_addc_u32 s5, s0, 0
	s_add_u32 s12, s1, 0x48480000
	s_addc_u32 s13, s0, 0
	s_add_u32 s14, s1, 0x4a480000
	s_addc_u32 s15, s0, 0
	s_add_u32 s19, s1, 0x4c0000
	s_addc_u32 s20, s0, 0
	s_add_u32 s21, s1, 0x35c80000
	s_addc_u32 s22, s0, 0
	s_lshl_b32 s0, s16, 11
	s_lshl_b32 s1, s76, 8
	v_lshlrev_b32_e32 v0, 2, v0
	s_add_i32 s23, s0, s1
	v_mov_b32_e32 v1, 0x3a27c5ac
	s_mov_b32 s24, 0xf800000
	v_mov_b32_e32 v2, 0x260
	s_waitcnt lgkmcnt(0)
	s_and_b32 s0, s23, 0x300
	v_add_u32_e32 v130, s0, v0
	v_lshlrev_b32_e32 v130, 2, v130
	global_load_dwordx4 v[134:137], v130, s[10:11]
	global_load_dwordx4 v[130:133], v130, s[8:9]
.LBB0_1879:
	s_ashr_i32 s6, s18, 2
	s_and_b32 s0, s23, 0x300
	v_add_u32_e32 v16, s0, v0
	s_ashr_i32 s7, s6, 31
	s_lshl_b64 s[0:1], s[6:7], 10
	v_ashrrev_i32_e32 v17, 31, v16
	v_lshl_add_u64 v[4:5], s[0:1], 0, v[16:17]
	v_lshl_add_u64 v[8:9], v[4:5], 2, s[4:5]
	v_lshlrev_b64 v[10:11], 1, v[4:5]
	s_waitcnt lgkmcnt(0)
	global_load_dwordx4 v[4:7], v[8:9], off
	s_lshl_b64 s[16:17], s[6:7], 6
	v_ashrrev_i32_e32 v18, 6, v16
	s_add_u32 s16, s19, s16
	v_ashrrev_i32_e32 v19, 31, v18
	s_addc_u32 s17, s20, s17
	v_lshl_add_u64 v[20:21], s[12:13], 0, v[10:11]
	v_lshl_add_u64 v[22:23], s[14:15], 0, v[10:11]
	s_nop 0
	v_lshl_add_u64 v[18:19], v[18:19], 2, s[16:17]
	global_load_dwordx2 v[20:21], v[20:21], off
	s_nop 0
	global_load_dwordx2 v[22:23], v[22:23], off
	s_nop 0
	global_load_dword v18, v[18:19], off
	s_lshl_b64 s[0:1], s[6:7], 12
	s_add_u32 s0, s21, s0
	s_addc_u32 s1, s22, s1
	s_add_i32 s6, s18, 0x800
	s_add_i32 s23, s23, 0x80000
	s_cmpk_lt_i32 s18, 0x7800
	s_mov_b32 s18, s6
	v_lshl_add_u64 v[16:17], v[16:17], 1, s[0:1]
	s_ashr_i32 s6, s18, 2
	s_and_b32 s0, s23, 0x300
	v_add_u32_e32 v48, s0, v0
	s_ashr_i32 s7, s6, 31
	s_lshl_b64 s[0:1], s[6:7], 10
	v_ashrrev_i32_e32 v49, 31, v48
	v_lshl_add_u64 v[36:37], s[0:1], 0, v[48:49]
	v_lshl_add_u64 v[40:41], v[36:37], 2, s[4:5]
	v_lshlrev_b64 v[42:43], 1, v[36:37]
	s_waitcnt lgkmcnt(0)
	global_load_dwordx4 v[36:39], v[40:41], off
	s_lshl_b64 s[16:17], s[6:7], 6
	v_ashrrev_i32_e32 v50, 6, v48
	s_add_u32 s16, s19, s16
	v_ashrrev_i32_e32 v51, 31, v50
	s_addc_u32 s17, s20, s17
	v_lshl_add_u64 v[52:53], s[12:13], 0, v[42:43]
	v_lshl_add_u64 v[54:55], s[14:15], 0, v[42:43]
	s_nop 0
	v_lshl_add_u64 v[50:51], v[50:51], 2, s[16:17]
	global_load_dwordx2 v[52:53], v[52:53], off
	s_nop 0
	global_load_dwordx2 v[54:55], v[54:55], off
	s_nop 0
	global_load_dword v50, v[50:51], off
	s_lshl_b64 s[0:1], s[6:7], 12
	s_add_u32 s0, s21, s0
	s_addc_u32 s1, s22, s1
	s_add_i32 s6, s18, 0x800
	s_add_i32 s23, s23, 0x80000
	s_cmpk_lt_i32 s18, 0x7800
	s_mov_b32 s18, s6
	v_lshl_add_u64 v[48:49], v[48:49], 1, s[0:1]
	s_ashr_i32 s6, s18, 2
	s_and_b32 s0, s23, 0x300
	v_add_u32_e32 v80, s0, v0
	s_ashr_i32 s7, s6, 31
	s_lshl_b64 s[0:1], s[6:7], 10
	v_ashrrev_i32_e32 v81, 31, v80
	v_lshl_add_u64 v[68:69], s[0:1], 0, v[80:81]
	v_lshl_add_u64 v[72:73], v[68:69], 2, s[4:5]
	v_lshlrev_b64 v[74:75], 1, v[68:69]
	s_waitcnt lgkmcnt(0)
	global_load_dwordx4 v[68:71], v[72:73], off
	s_lshl_b64 s[16:17], s[6:7], 6
	v_ashrrev_i32_e32 v82, 6, v80
	s_add_u32 s16, s19, s16
	v_ashrrev_i32_e32 v83, 31, v82
	s_addc_u32 s17, s20, s17
	v_lshl_add_u64 v[84:85], s[12:13], 0, v[74:75]
	v_lshl_add_u64 v[86:87], s[14:15], 0, v[74:75]
	s_nop 0
	v_lshl_add_u64 v[82:83], v[82:83], 2, s[16:17]
	global_load_dwordx2 v[84:85], v[84:85], off
	s_nop 0
	global_load_dwordx2 v[86:87], v[86:87], off
	s_nop 0
	global_load_dword v82, v[82:83], off
	s_lshl_b64 s[0:1], s[6:7], 12
	s_add_u32 s0, s21, s0
	s_addc_u32 s1, s22, s1
	s_add_i32 s6, s18, 0x800
	s_add_i32 s23, s23, 0x80000
	s_cmpk_lt_i32 s18, 0x7800
	s_mov_b32 s18, s6
	v_lshl_add_u64 v[80:81], v[80:81], 1, s[0:1]
	s_ashr_i32 s6, s18, 2
	s_and_b32 s0, s23, 0x300
	v_add_u32_e32 v112, s0, v0
	s_ashr_i32 s7, s6, 31
	s_lshl_b64 s[0:1], s[6:7], 10
	v_ashrrev_i32_e32 v113, 31, v112
	v_lshl_add_u64 v[100:101], s[0:1], 0, v[112:113]
	v_lshl_add_u64 v[104:105], v[100:101], 2, s[4:5]
	v_lshlrev_b64 v[106:107], 1, v[100:101]
	s_waitcnt lgkmcnt(0)
	global_load_dwordx4 v[100:103], v[104:105], off
	s_lshl_b64 s[16:17], s[6:7], 6
	v_ashrrev_i32_e32 v114, 6, v112
	s_add_u32 s16, s19, s16
	v_ashrrev_i32_e32 v115, 31, v114
	s_addc_u32 s17, s20, s17
	v_lshl_add_u64 v[116:117], s[12:13], 0, v[106:107]
	v_lshl_add_u64 v[118:119], s[14:15], 0, v[106:107]
	s_nop 0
	v_lshl_add_u64 v[114:115], v[114:115], 2, s[16:17]
	global_load_dwordx2 v[116:117], v[116:117], off
	s_nop 0
	global_load_dwordx2 v[118:119], v[118:119], off
	s_nop 0
	global_load_dword v114, v[114:115], off
	s_lshl_b64 s[0:1], s[6:7], 12
	s_add_u32 s0, s21, s0
	s_addc_u32 s1, s22, s1
	s_add_i32 s6, s18, 0x800
	s_add_i32 s23, s23, 0x80000
	s_cmpk_lt_i32 s18, 0x7800
	s_mov_b32 s18, s6
	v_lshl_add_u64 v[112:113], v[112:113], 1, s[0:1]
	s_waitcnt vmcnt(15)
	v_mov_b32_e32 v24, v5
	v_mov_b32_e32 v25, v6
	v_mov_b32_e32 v26, v4
	v_mov_b32_e32 v27, v7
	v_pk_add_f32 v[24:25], v[24:25], v[26:27]
	s_waitcnt vmcnt(14)
	v_lshlrev_b32_e32 v26, 16, v20
	v_add_f32_e32 v3, v24, v25
	v_and_b32_e32 v27, 0xffff0000, v20
	v_lshlrev_b32_e32 v20, 16, v21
	v_add_f32_dpp v3, v3, v3 quad_perm:[1,0,3,2] row_mask:0xf bank_mask:0xf bound_ctrl:1
	v_and_b32_e32 v21, 0xffff0000, v21
	s_waitcnt vmcnt(13)
	v_lshlrev_b32_e32 v28, 16, v22
	v_add_f32_dpp v3, v3, v3 quad_perm:[2,3,0,1] row_mask:0xf bank_mask:0xf bound_ctrl:1
	v_and_b32_e32 v29, 0xffff0000, v22
	v_lshlrev_b32_e32 v22, 16, v23
	v_add_f32_dpp v3, v3, v3 row_half_mirror row_mask:0xf bank_mask:0xf bound_ctrl:1
	v_and_b32_e32 v23, 0xffff0000, v23
	s_nop 0
	v_add_f32_dpp v3, v3, v3 row_mirror row_mask:0xf bank_mask:0xf bound_ctrl:1
	v_fmamk_f32 v5, v3, 0xbc800000, v5
	v_fmamk_f32 v4, v3, 0xbc800000, v4
	v_fmamk_f32 v7, v3, 0xbc800000, v7
	v_fmac_f32_e32 v6, 0xbc800000, v3
	v_pk_mul_f32 v[24:25], v[6:7], v[6:7]
	v_pk_mul_f32 v[30:31], v[4:5], v[4:5]
	s_nop 0
	v_pk_mov_b32 v[32:33], v[30:31], v[24:25] op_sel:[1,0]
	v_mov_b32_e32 v31, v25
	v_pk_add_f32 v[24:25], v[32:33], v[30:31]
	s_nop 0
	v_add_f32_e32 v3, v24, v25
	s_nop 1
	v_add_f32_dpp v3, v3, v3 quad_perm:[1,0,3,2] row_mask:0xf bank_mask:0xf bound_ctrl:1
	s_nop 1
	v_add_f32_dpp v3, v3, v3 quad_perm:[2,3,0,1] row_mask:0xf bank_mask:0xf bound_ctrl:1
	s_nop 1
	v_add_f32_dpp v3, v3, v3 row_half_mirror row_mask:0xf bank_mask:0xf bound_ctrl:1
	s_nop 1
	v_add_f32_dpp v3, v3, v3 row_mirror row_mask:0xf bank_mask:0xf bound_ctrl:1
	v_fmamk_f32 v3, v3, 0x3c800000, v1
	v_mul_f32_e32 v19, 0x4f800000, v3
	v_cmp_gt_f32_e32 vcc, s24, v3
	s_nop 1
	v_cndmask_b32_e32 v3, v3, v19, vcc
	v_sqrt_f32_e32 v19, v3
	s_nop 0
	v_add_u32_e32 v24, -1, v19
	v_add_u32_e32 v25, 1, v19
	v_fma_f32 v30, -v24, v19, v3
	v_fma_f32 v31, -v25, v19, v3
	v_cmp_ge_f32_e64 s[6:7], 0, v30
	s_nop 1
	v_cndmask_b32_e64 v19, v19, v24, s[6:7]
	v_cmp_lt_f32_e64 s[6:7], 0, v31
	s_nop 1
	v_cndmask_b32_e64 v19, v19, v25, s[6:7]
	v_mul_f32_e32 v24, 0x37800000, v19
	v_cndmask_b32_e32 v19, v19, v24, vcc
	v_cmp_class_f32_e32 vcc, v3, v2
	s_nop 1
	v_cndmask_b32_e32 v3, v19, v3, vcc
	v_div_scale_f32 v19, s[0:1], v3, v3, 1.0
	v_rcp_f32_e32 v25, v19
	v_div_scale_f32 v24, vcc, 1.0, v3, 1.0
	v_fma_f32 v30, -v19, v25, 1.0
	v_fmac_f32_e32 v25, v30, v25
	v_mul_f32_e32 v30, v24, v25
	v_fma_f32 v31, -v19, v30, v24
	v_fmac_f32_e32 v30, v31, v25
	v_fma_f32 v19, -v19, v30, v24
	v_div_fmas_f32 v19, v19, v25, v30
	v_div_fixup_f32 v24, v19, v3, 1.0
	v_pk_mul_f32 v[4:5], v[4:5], v[24:25] op_sel_hi:[1,0]
	v_pk_mul_f32 v[6:7], v[6:7], v[24:25] op_sel_hi:[1,0]
	v_pk_fma_f32 v[4:5], v[130:131], v[4:5], v[134:135]
	v_pk_fma_f32 v[6:7], v[132:133], v[6:7], v[136:137]
	s_waitcnt vmcnt(12)
	v_pk_fma_f32 v[4:5], v[18:19], v[26:27], v[4:5] op_sel_hi:[0,1,1]
	v_pk_fma_f32 v[6:7], v[18:19], v[20:21], v[6:7] op_sel_hi:[0,1,1]
	v_pk_mul_f32 v[6:7], v[6:7], v[22:23]
	v_pk_mul_f32 v[4:5], v[4:5], v[28:29]
	s_nop 0
	v_cvt_pk_bf16_f32 v4, v4, v5
	v_cvt_pk_bf16_f32 v5, v6, v7
	global_store_dwordx2 v[16:17], v[4:5], off
	s_waitcnt vmcnt(12)
	v_mov_b32_e32 v56, v37
	v_mov_b32_e32 v57, v38
	v_mov_b32_e32 v58, v36
	v_mov_b32_e32 v59, v39
	v_pk_add_f32 v[56:57], v[56:57], v[58:59]
	s_waitcnt vmcnt(11)
	v_lshlrev_b32_e32 v58, 16, v52
	v_add_f32_e32 v35, v56, v57
	v_and_b32_e32 v59, 0xffff0000, v52
	v_lshlrev_b32_e32 v52, 16, v53
	v_add_f32_dpp v35, v35, v35 quad_perm:[1,0,3,2] row_mask:0xf bank_mask:0xf bound_ctrl:1
	v_and_b32_e32 v53, 0xffff0000, v53
	s_waitcnt vmcnt(10)
	v_lshlrev_b32_e32 v60, 16, v54
	v_add_f32_dpp v35, v35, v35 quad_perm:[2,3,0,1] row_mask:0xf bank_mask:0xf bound_ctrl:1
	v_and_b32_e32 v61, 0xffff0000, v54
	v_lshlrev_b32_e32 v54, 16, v55
	v_add_f32_dpp v35, v35, v35 row_half_mirror row_mask:0xf bank_mask:0xf bound_ctrl:1
	v_and_b32_e32 v55, 0xffff0000, v55
	s_nop 0
	v_add_f32_dpp v35, v35, v35 row_mirror row_mask:0xf bank_mask:0xf bound_ctrl:1
	v_fmamk_f32 v37, v35, 0xbc800000, v37
	v_fmamk_f32 v36, v35, 0xbc800000, v36
	v_fmamk_f32 v39, v35, 0xbc800000, v39
	v_fmac_f32_e32 v38, 0xbc800000, v35
	v_pk_mul_f32 v[56:57], v[38:39], v[38:39]
	v_pk_mul_f32 v[62:63], v[36:37], v[36:37]
	s_nop 0
	v_pk_mov_b32 v[64:65], v[62:63], v[56:57] op_sel:[1,0]
	v_mov_b32_e32 v63, v57
	v_pk_add_f32 v[56:57], v[64:65], v[62:63]
	s_nop 0
	v_add_f32_e32 v35, v56, v57
	s_nop 1
	v_add_f32_dpp v35, v35, v35 quad_perm:[1,0,3,2] row_mask:0xf bank_mask:0xf bound_ctrl:1
	s_nop 1
	v_add_f32_dpp v35, v35, v35 quad_perm:[2,3,0,1] row_mask:0xf bank_mask:0xf bound_ctrl:1
	s_nop 1
	v_add_f32_dpp v35, v35, v35 row_half_mirror row_mask:0xf bank_mask:0xf bound_ctrl:1
	s_nop 1
	v_add_f32_dpp v35, v35, v35 row_mirror row_mask:0xf bank_mask:0xf bound_ctrl:1
	v_fmamk_f32 v35, v35, 0x3c800000, v1
	v_mul_f32_e32 v51, 0x4f800000, v35
	v_cmp_gt_f32_e32 vcc, s24, v35
	s_nop 1
	v_cndmask_b32_e32 v35, v35, v51, vcc
	v_sqrt_f32_e32 v51, v35
	s_nop 0
	v_add_u32_e32 v56, -1, v51
	v_add_u32_e32 v57, 1, v51
	v_fma_f32 v62, -v56, v51, v35
	v_fma_f32 v63, -v57, v51, v35
	v_cmp_ge_f32_e64 s[6:7], 0, v62
	s_nop 1
	v_cndmask_b32_e64 v51, v51, v56, s[6:7]
	v_cmp_lt_f32_e64 s[6:7], 0, v63
	s_nop 1
	v_cndmask_b32_e64 v51, v51, v57, s[6:7]
	v_mul_f32_e32 v56, 0x37800000, v51
	v_cndmask_b32_e32 v51, v51, v56, vcc
	v_cmp_class_f32_e32 vcc, v35, v2
	s_nop 1
	v_cndmask_b32_e32 v35, v51, v35, vcc
	v_div_scale_f32 v51, s[0:1], v35, v35, 1.0
	v_rcp_f32_e32 v57, v51
	v_div_scale_f32 v56, vcc, 1.0, v35, 1.0
	v_fma_f32 v62, -v51, v57, 1.0
	v_fmac_f32_e32 v57, v62, v57
	v_mul_f32_e32 v62, v56, v57
	v_fma_f32 v63, -v51, v62, v56
	v_fmac_f32_e32 v62, v63, v57
	v_fma_f32 v51, -v51, v62, v56
	v_div_fmas_f32 v51, v51, v57, v62
	v_div_fixup_f32 v56, v51, v35, 1.0
	v_pk_mul_f32 v[36:37], v[36:37], v[56:57] op_sel_hi:[1,0]
	v_pk_mul_f32 v[38:39], v[38:39], v[56:57] op_sel_hi:[1,0]
	v_pk_fma_f32 v[36:37], v[130:131], v[36:37], v[134:135]
	v_pk_fma_f32 v[38:39], v[132:133], v[38:39], v[136:137]
	s_waitcnt vmcnt(9)
	v_pk_fma_f32 v[36:37], v[50:51], v[58:59], v[36:37] op_sel_hi:[0,1,1]
	v_pk_fma_f32 v[38:39], v[50:51], v[52:53], v[38:39] op_sel_hi:[0,1,1]
	v_pk_mul_f32 v[38:39], v[38:39], v[54:55]
	v_pk_mul_f32 v[36:37], v[36:37], v[60:61]
	s_nop 0
	v_cvt_pk_bf16_f32 v36, v36, v37
	v_cvt_pk_bf16_f32 v37, v38, v39
	global_store_dwordx2 v[48:49], v[36:37], off
	s_waitcnt vmcnt(9)
	v_mov_b32_e32 v88, v69
	v_mov_b32_e32 v89, v70
	v_mov_b32_e32 v90, v68
	v_mov_b32_e32 v91, v71
	v_pk_add_f32 v[88:89], v[88:89], v[90:91]
	s_waitcnt vmcnt(8)
	v_lshlrev_b32_e32 v90, 16, v84
	v_add_f32_e32 v67, v88, v89
	v_and_b32_e32 v91, 0xffff0000, v84
	v_lshlrev_b32_e32 v84, 16, v85
	v_add_f32_dpp v67, v67, v67 quad_perm:[1,0,3,2] row_mask:0xf bank_mask:0xf bound_ctrl:1
	v_and_b32_e32 v85, 0xffff0000, v85
	s_waitcnt vmcnt(7)
	v_lshlrev_b32_e32 v92, 16, v86
	v_add_f32_dpp v67, v67, v67 quad_perm:[2,3,0,1] row_mask:0xf bank_mask:0xf bound_ctrl:1
	v_and_b32_e32 v93, 0xffff0000, v86
	v_lshlrev_b32_e32 v86, 16, v87
	v_add_f32_dpp v67, v67, v67 row_half_mirror row_mask:0xf bank_mask:0xf bound_ctrl:1
	v_and_b32_e32 v87, 0xffff0000, v87
	s_nop 0
	v_add_f32_dpp v67, v67, v67 row_mirror row_mask:0xf bank_mask:0xf bound_ctrl:1
	v_fmamk_f32 v69, v67, 0xbc800000, v69
	v_fmamk_f32 v68, v67, 0xbc800000, v68
	v_fmamk_f32 v71, v67, 0xbc800000, v71
	v_fmac_f32_e32 v70, 0xbc800000, v67
	v_pk_mul_f32 v[88:89], v[70:71], v[70:71]
	v_pk_mul_f32 v[94:95], v[68:69], v[68:69]
	s_nop 0
	v_pk_mov_b32 v[96:97], v[94:95], v[88:89] op_sel:[1,0]
	v_mov_b32_e32 v95, v89
	v_pk_add_f32 v[88:89], v[96:97], v[94:95]
	s_nop 0
	v_add_f32_e32 v67, v88, v89
	s_nop 1
	v_add_f32_dpp v67, v67, v67 quad_perm:[1,0,3,2] row_mask:0xf bank_mask:0xf bound_ctrl:1
	s_nop 1
	v_add_f32_dpp v67, v67, v67 quad_perm:[2,3,0,1] row_mask:0xf bank_mask:0xf bound_ctrl:1
	s_nop 1
	v_add_f32_dpp v67, v67, v67 row_half_mirror row_mask:0xf bank_mask:0xf bound_ctrl:1
	s_nop 1
	v_add_f32_dpp v67, v67, v67 row_mirror row_mask:0xf bank_mask:0xf bound_ctrl:1
	v_fmamk_f32 v67, v67, 0x3c800000, v1
	v_mul_f32_e32 v83, 0x4f800000, v67
	v_cmp_gt_f32_e32 vcc, s24, v67
	s_nop 1
	v_cndmask_b32_e32 v67, v67, v83, vcc
	v_sqrt_f32_e32 v83, v67
	s_nop 0
	v_add_u32_e32 v88, -1, v83
	v_add_u32_e32 v89, 1, v83
	v_fma_f32 v94, -v88, v83, v67
	v_fma_f32 v95, -v89, v83, v67
	v_cmp_ge_f32_e64 s[6:7], 0, v94
	s_nop 1
	v_cndmask_b32_e64 v83, v83, v88, s[6:7]
	v_cmp_lt_f32_e64 s[6:7], 0, v95
	s_nop 1
	v_cndmask_b32_e64 v83, v83, v89, s[6:7]
	v_mul_f32_e32 v88, 0x37800000, v83
	v_cndmask_b32_e32 v83, v83, v88, vcc
	v_cmp_class_f32_e32 vcc, v67, v2
	s_nop 1
	v_cndmask_b32_e32 v67, v83, v67, vcc
	v_div_scale_f32 v83, s[0:1], v67, v67, 1.0
	v_rcp_f32_e32 v89, v83
	v_div_scale_f32 v88, vcc, 1.0, v67, 1.0
	v_fma_f32 v94, -v83, v89, 1.0
	v_fmac_f32_e32 v89, v94, v89
	v_mul_f32_e32 v94, v88, v89
	v_fma_f32 v95, -v83, v94, v88
	v_fmac_f32_e32 v94, v95, v89
	v_fma_f32 v83, -v83, v94, v88
	v_div_fmas_f32 v83, v83, v89, v94
	v_div_fixup_f32 v88, v83, v67, 1.0
	v_pk_mul_f32 v[68:69], v[68:69], v[88:89] op_sel_hi:[1,0]
	v_pk_mul_f32 v[70:71], v[70:71], v[88:89] op_sel_hi:[1,0]
	v_pk_fma_f32 v[68:69], v[130:131], v[68:69], v[134:135]
	v_pk_fma_f32 v[70:71], v[132:133], v[70:71], v[136:137]
	s_waitcnt vmcnt(6)
	v_pk_fma_f32 v[68:69], v[82:83], v[90:91], v[68:69] op_sel_hi:[0,1,1]
	v_pk_fma_f32 v[70:71], v[82:83], v[84:85], v[70:71] op_sel_hi:[0,1,1]
	v_pk_mul_f32 v[70:71], v[70:71], v[86:87]
	v_pk_mul_f32 v[68:69], v[68:69], v[92:93]
	s_nop 0
	v_cvt_pk_bf16_f32 v68, v68, v69
	v_cvt_pk_bf16_f32 v69, v70, v71
	global_store_dwordx2 v[80:81], v[68:69], off
	s_waitcnt vmcnt(6)
	v_mov_b32_e32 v120, v101
	v_mov_b32_e32 v121, v102
	v_mov_b32_e32 v122, v100
	v_mov_b32_e32 v123, v103
	v_pk_add_f32 v[120:121], v[120:121], v[122:123]
	s_waitcnt vmcnt(5)
	v_lshlrev_b32_e32 v122, 16, v116
	v_add_f32_e32 v99, v120, v121
	v_and_b32_e32 v123, 0xffff0000, v116
	v_lshlrev_b32_e32 v116, 16, v117
	v_add_f32_dpp v99, v99, v99 quad_perm:[1,0,3,2] row_mask:0xf bank_mask:0xf bound_ctrl:1
	v_and_b32_e32 v117, 0xffff0000, v117
	s_waitcnt vmcnt(4)
	v_lshlrev_b32_e32 v124, 16, v118
	v_add_f32_dpp v99, v99, v99 quad_perm:[2,3,0,1] row_mask:0xf bank_mask:0xf bound_ctrl:1
	v_and_b32_e32 v125, 0xffff0000, v118
	v_lshlrev_b32_e32 v118, 16, v119
	v_add_f32_dpp v99, v99, v99 row_half_mirror row_mask:0xf bank_mask:0xf bound_ctrl:1
	v_and_b32_e32 v119, 0xffff0000, v119
	s_nop 0
	v_add_f32_dpp v99, v99, v99 row_mirror row_mask:0xf bank_mask:0xf bound_ctrl:1
	v_fmamk_f32 v101, v99, 0xbc800000, v101
	v_fmamk_f32 v100, v99, 0xbc800000, v100
	v_fmamk_f32 v103, v99, 0xbc800000, v103
	v_fmac_f32_e32 v102, 0xbc800000, v99
	v_pk_mul_f32 v[120:121], v[102:103], v[102:103]
	v_pk_mul_f32 v[126:127], v[100:101], v[100:101]
	s_nop 0
	v_pk_mov_b32 v[128:129], v[126:127], v[120:121] op_sel:[1,0]
	v_mov_b32_e32 v127, v121
	v_pk_add_f32 v[120:121], v[128:129], v[126:127]
	s_nop 0
	v_add_f32_e32 v99, v120, v121
	s_nop 1
	v_add_f32_dpp v99, v99, v99 quad_perm:[1,0,3,2] row_mask:0xf bank_mask:0xf bound_ctrl:1
	s_nop 1
	v_add_f32_dpp v99, v99, v99 quad_perm:[2,3,0,1] row_mask:0xf bank_mask:0xf bound_ctrl:1
	s_nop 1
	v_add_f32_dpp v99, v99, v99 row_half_mirror row_mask:0xf bank_mask:0xf bound_ctrl:1
	s_nop 1
	v_add_f32_dpp v99, v99, v99 row_mirror row_mask:0xf bank_mask:0xf bound_ctrl:1
	v_fmamk_f32 v99, v99, 0x3c800000, v1
	v_mul_f32_e32 v115, 0x4f800000, v99
	v_cmp_gt_f32_e32 vcc, s24, v99
	s_nop 1
	v_cndmask_b32_e32 v99, v99, v115, vcc
	v_sqrt_f32_e32 v115, v99
	s_nop 0
	v_add_u32_e32 v120, -1, v115
	v_add_u32_e32 v121, 1, v115
	v_fma_f32 v126, -v120, v115, v99
	v_fma_f32 v127, -v121, v115, v99
	v_cmp_ge_f32_e64 s[6:7], 0, v126
	s_nop 1
	v_cndmask_b32_e64 v115, v115, v120, s[6:7]
	v_cmp_lt_f32_e64 s[6:7], 0, v127
	s_nop 1
	v_cndmask_b32_e64 v115, v115, v121, s[6:7]
	v_mul_f32_e32 v120, 0x37800000, v115
	v_cndmask_b32_e32 v115, v115, v120, vcc
	v_cmp_class_f32_e32 vcc, v99, v2
	s_nop 1
	v_cndmask_b32_e32 v99, v115, v99, vcc
	v_div_scale_f32 v115, s[0:1], v99, v99, 1.0
	v_rcp_f32_e32 v121, v115
	v_div_scale_f32 v120, vcc, 1.0, v99, 1.0
	v_fma_f32 v126, -v115, v121, 1.0
	v_fmac_f32_e32 v121, v126, v121
	v_mul_f32_e32 v126, v120, v121
	v_fma_f32 v127, -v115, v126, v120
	v_fmac_f32_e32 v126, v127, v121
	v_fma_f32 v115, -v115, v126, v120
	v_div_fmas_f32 v115, v115, v121, v126
	v_div_fixup_f32 v120, v115, v99, 1.0
	v_pk_mul_f32 v[100:101], v[100:101], v[120:121] op_sel_hi:[1,0]
	v_pk_mul_f32 v[102:103], v[102:103], v[120:121] op_sel_hi:[1,0]
	v_pk_fma_f32 v[100:101], v[130:131], v[100:101], v[134:135]
	v_pk_fma_f32 v[102:103], v[132:133], v[102:103], v[136:137]
	s_waitcnt vmcnt(3)
	v_pk_fma_f32 v[100:101], v[114:115], v[122:123], v[100:101] op_sel_hi:[0,1,1]
	v_pk_fma_f32 v[102:103], v[114:115], v[116:117], v[102:103] op_sel_hi:[0,1,1]
	v_pk_mul_f32 v[102:103], v[102:103], v[118:119]
	v_pk_mul_f32 v[100:101], v[100:101], v[124:125]
	s_nop 0
	v_cvt_pk_bf16_f32 v100, v100, v101
	v_cvt_pk_bf16_f32 v101, v102, v103
	global_store_dwordx2 v[112:113], v[100:101], off
	s_cbranch_scc1 .LBB0_1879
	v_readlane_b32 s0, v254, 18
	v_readlane_b32 s1, v254, 19
	s_load_dwordx2 s[6:7], s[0:1], 0x188
